# spatial prologue rewritten by hand: all K V Q loads issued up front then LDS image writes; outproj block remap for XCD locality
# baseline (speedup 1.0000x reference)
_Z9k_spatialPKDF16_S0_S0_PfPDF16_:
	s_load_dwordx4 s[4:7], s[0:1], 0x0
	s_load_dwordx2 s[10:11], s[0:1], 0x10
	s_mul_hi_i32 s9, s2, 0x3140
	s_mul_i32 s8, s2, 0x3140
	s_lshl_b64 s[8:9], s[8:9], 1
	v_and_b32_e32 v2, 7, v0
	v_lshrrev_b32_e32 v3, 3, v0
	v_lshlrev_b32_e32 v10, 4, v2
	v_lshl_or_b32 v4, v3, 7, v10
	v_add_u32_e32 v5, 0x1c00, v4
	v_add_u32_e32 v6, 0x3800, v4
	v_add_u32_e32 v7, 0x5400, v4
	v_lshrrev_b32_e32 v8, 1, v0
	v_and_b32_e32 v132, 31, v0
	v_and_b32_e32 v133, 0xe0, v8
	v_or_b32_e32 v135, v133, v132
	s_movk_i32 s3, 0xc5
	v_mov_b32_e32 v8, 0xc4
	v_cmp_gt_u32_e64 s[12:13], s3, v135
	v_bfe_u32 v1, v0, 5, 1
	v_mov_b32_e32 v131, 0
	v_lshlrev_b32_e32 v130, 4, v1
	s_nop 0
	v_cndmask_b32_e64 v134, v8, v135, s[12:13]
	v_lshl_or_b32 v9, v134, 7, v130
	s_movk_i32 s3, 0xe8
	v_cmp_gt_u32_e32 vcc, s3, v0
	v_or_b32_e32 v14, 0x6200, v10
	s_nop 1
	v_cndmask_b32_e32 v7, v14, v7, vcc
	s_waitcnt lgkmcnt(0)
	s_add_u32 s6, s6, s8
	s_addc_u32 s7, s7, s9
	s_add_u32 s10, s10, s8
	s_addc_u32 s11, s11, s9
	s_add_u32 s4, s4, s8
	s_addc_u32 s5, s5, s9
	global_load_dwordx4 v[18:21], v4, s[6:7] nt
	global_load_dwordx4 v[22:25], v4, s[10:11] nt
	global_load_dwordx4 v[26:29], v5, s[6:7] nt
	global_load_dwordx4 v[30:33], v5, s[10:11] nt
	global_load_dwordx4 v[34:37], v6, s[6:7] nt
	global_load_dwordx4 v[38:41], v6, s[10:11] nt
	global_load_dwordx4 v[42:45], v7, s[6:7] nt
	global_load_dwordx4 v[46:49], v7, s[10:11] nt
	global_load_dwordx4 v[118:121], v9, s[4:5] nt
	global_load_dwordx4 v[114:117], v9, s[4:5] offset:32 nt
	global_load_dwordx4 v[126:129], v9, s[4:5] offset:64 nt
	global_load_dwordx4 v[122:125], v9, s[4:5] offset:96 nt
	s_movk_i32 s3, 0x90
	s_movk_i32 s6, 0x1c8
	v_lshlrev_b32_e32 v11, 3, v2
	v_mul_u32_u24_e32 v16, 0x1c8, v11
	v_mad_u32_u24 v12, v3, s3, v10
	v_lshl_add_u32 v13, v3, 1, v16
	v_mad_u32_u24 v152, v132, s3, v130
	s_waitcnt vmcnt(11)
	ds_write_b128 v12, v[18:21] offset:0
	s_waitcnt vmcnt(10)
	ds_write_b16 v13, v22 offset:32256
	ds_write_b16_d16_hi v13, v22 offset:32712
	ds_write_b16 v13, v23 offset:33168
	ds_write_b16_d16_hi v13, v23 offset:33624
	ds_write_b16 v13, v24 offset:34080
	ds_write_b16_d16_hi v13, v24 offset:34536
	ds_write_b16 v13, v25 offset:34992
	ds_write_b16_d16_hi v13, v25 offset:35448
	s_waitcnt vmcnt(9)
	ds_write_b128 v12, v[26:29] offset:8064
	s_waitcnt vmcnt(8)
	ds_write_b16 v13, v30 offset:32368
	ds_write_b16_d16_hi v13, v30 offset:32824
	ds_write_b16 v13, v31 offset:33280
	ds_write_b16_d16_hi v13, v31 offset:33736
	ds_write_b16 v13, v32 offset:34192
	ds_write_b16_d16_hi v13, v32 offset:34648
	ds_write_b16 v13, v33 offset:35104
	ds_write_b16_d16_hi v13, v33 offset:35560
	s_waitcnt vmcnt(7)
	ds_write_b128 v12, v[34:37] offset:16128
	s_waitcnt vmcnt(6)
	ds_write_b16 v13, v38 offset:32480
	ds_write_b16_d16_hi v13, v38 offset:32936
	ds_write_b16 v13, v39 offset:33392
	ds_write_b16_d16_hi v13, v39 offset:33848
	ds_write_b16 v13, v40 offset:34304
	ds_write_b16_d16_hi v13, v40 offset:34760
	ds_write_b16 v13, v41 offset:35216
	ds_write_b16_d16_hi v13, v41 offset:35672
	s_waitcnt vmcnt(5)
	v_cndmask_b32_e32 v42, 0, v42, vcc
	v_cndmask_b32_e32 v43, 0, v43, vcc
	v_cndmask_b32_e32 v44, 0, v44, vcc
	v_cndmask_b32_e32 v45, 0, v45, vcc
	ds_write_b128 v12, v[42:45] offset:24192
	s_waitcnt vmcnt(4)
	v_cndmask_b32_e32 v46, 0, v46, vcc
	v_cndmask_b32_e32 v47, 0, v47, vcc
	v_cndmask_b32_e32 v48, 0, v48, vcc
	v_cndmask_b32_e32 v49, 0, v49, vcc
	ds_write_b16 v13, v46 offset:32592
	ds_write_b16_d16_hi v13, v46 offset:33048
	ds_write_b16 v13, v47 offset:33504
	ds_write_b16_d16_hi v13, v47 offset:33960
	ds_write_b16 v13, v48 offset:34416
	ds_write_b16_d16_hi v13, v48 offset:34872
	ds_write_b16 v13, v49 offset:35328
	ds_write_b16_d16_hi v13, v49 offset:35784
	s_mov_b64 s[4:5], s[12:13]
	s_waitcnt lgkmcnt(0)
	s_barrier
	ds_read_b128 v[2:5], v152
	ds_read_b128 v[6:9], v152 offset:32
	v_cmp_eq_u32_e64 s[6:7], 0, v1
	s_mov_b32 s3, 0xf149f2ca
	v_mov_b32_e32 v168, 0xf011accb
	s_load_dwordx2 s[8:9], s[0:1], 0x20
	s_waitcnt vmcnt(3) lgkmcnt(0)
	v_mfma_f32_32x32x16_f16 v[98:113], v[2:5], v[118:121], 0
	ds_read_b128 v[2:5], v152 offset:4608
	ds_read_b128 v[10:13], v152 offset:4640
	s_waitcnt lgkmcnt(1)
	v_mfma_f32_32x32x16_f16 v[66:81], v[2:5], v[118:121], 0
	ds_read_b128 v[2:5], v152 offset:9216
	ds_read_b128 v[14:17], v152 offset:9248
	s_waitcnt lgkmcnt(1)
	v_mfma_f32_32x32x16_f16 v[50:65], v[2:5], v[118:121], 0
	ds_read_b128 v[2:5], v152 offset:13824
	ds_read_b128 v[18:21], v152 offset:13856
	s_waitcnt vmcnt(2)
	v_mfma_f32_32x32x16_f16 v[98:113], v[6:9], v[114:117], v[98:113]
	s_waitcnt lgkmcnt(1)
	v_mfma_f32_32x32x16_f16 v[34:49], v[2:5], v[118:121], 0
	ds_read_b128 v[2:5], v152 offset:64
	ds_read_b128 v[6:9], v152 offset:96
	v_mfma_f32_32x32x16_f16 v[66:81], v[10:13], v[114:117], v[66:81]
	v_mfma_f32_32x32x16_f16 v[50:65], v[14:17], v[114:117], v[50:65]
	s_waitcnt vmcnt(1) lgkmcnt(1)
	v_mfma_f32_32x32x16_f16 v[98:113], v[2:5], v[126:129], v[98:113]
	ds_read_b128 v[2:5], v152 offset:4672
	ds_read_b128 v[10:13], v152 offset:4704
	v_mfma_f32_32x32x16_f16 v[34:49], v[18:21], v[114:117], v[34:49]
	s_waitcnt lgkmcnt(1)
	v_mfma_f32_32x32x16_f16 v[66:81], v[2:5], v[126:129], v[66:81]
	ds_read_b128 v[2:5], v152 offset:9280
	ds_read_b128 v[14:17], v152 offset:9312
	s_waitcnt lgkmcnt(1)
	v_mfma_f32_32x32x16_f16 v[50:65], v[2:5], v[126:129], v[50:65]
	s_waitcnt vmcnt(0)
	v_mfma_f32_32x32x16_f16 v[98:113], v[6:9], v[122:125], v[98:113]
	ds_read_b128 v[2:5], v152 offset:13888
	ds_read_b128 v[6:9], v152 offset:13920
	s_waitcnt lgkmcnt(1)
	v_mfma_f32_32x32x16_f16 v[34:49], v[2:5], v[126:129], v[34:49]
	ds_read_b128 v[2:5], v152 offset:18432
	ds_read_b128 v[82:85], v152 offset:18464
	s_waitcnt lgkmcnt(1)
	v_mfma_f32_32x32x16_f16 v[18:33], v[2:5], v[118:121], 0
	ds_read_b128 v[2:5], v152 offset:27648
	ds_read_b128 v[86:89], v152 offset:27680
	v_mfma_f32_32x32x16_f16 v[66:81], v[10:13], v[122:125], v[66:81]
	v_mfma_f32_32x32x16_f16 v[50:65], v[14:17], v[122:125], v[50:65]
	v_mfma_f32_32x32x16_f16 v[34:49], v[6:9], v[122:125], v[34:49]
	s_waitcnt lgkmcnt(1)
	v_mfma_f32_32x32x16_f16 v[2:17], v[2:5], v[118:121], 0
	s_waitcnt lgkmcnt(0)
	v_mfma_f32_32x32x16_f16 v[2:17], v[86:89], v[114:117], v[2:17]
	ds_read_b128 v[86:89], v152 offset:27712
	ds_read_b128 v[90:93], v152 offset:18496
	ds_read_b128 v[94:97], v152 offset:18528
	ds_read_b128 v[136:139], v152 offset:23040
	ds_read_b128 v[140:143], v152 offset:23072
	ds_read_b128 v[144:147], v152 offset:27744
	ds_read_b128 v[148:151], v152 offset:23104
	ds_read_b128 v[152:155], v152 offset:23136
	s_waitcnt lgkmcnt(7)
	v_mfma_f32_32x32x16_f16 v[2:17], v[86:89], v[126:129], v[2:17]
	v_mbcnt_lo_u32_b32 v86, -1, 0
	v_mbcnt_hi_u32_b32 v86, -1, v86
	v_and_b32_e32 v87, 64, v86
	v_add_u32_e32 v87, 64, v87
	v_xor_b32_e32 v88, 32, v86
	v_cmp_lt_i32_e32 vcc, v88, v87
	s_waitcnt lgkmcnt(2)
	v_mfma_f32_32x32x16_f16 v[2:17], v[144:147], v[122:125], v[2:17]
	v_mfma_f32_32x32x16_f16 v[18:33], v[82:85], v[114:117], v[18:33]
	s_nop 10
	v_mov_b32_e32 v7, 0xf149f2ca
	v_cndmask_b32_e64 v5, v7, v5, s[6:7]
	v_cndmask_b32_e64 v4, v7, v4, s[6:7]
	v_cndmask_b32_e64 v3, v7, v3, s[6:7]
	v_max_f32_e32 v7, v98, v98
	v_max_f32_e32 v7, 0xf149f2ca, v7
	v_max3_f32 v7, v7, v99, v100
	v_mfma_f32_32x32x16_f16 v[18:33], v[90:93], v[126:129], v[18:33]
	v_max3_f32 v7, v7, v101, v102
	v_max3_f32 v7, v7, v103, v104
	v_max3_f32 v7, v7, v105, v106
	v_max3_f32 v7, v7, v107, v108
	v_max3_f32 v7, v7, v109, v110
	v_max3_f32 v7, v7, v111, v112
	v_cndmask_b32_e32 v6, v86, v88, vcc
	v_max3_f32 v7, v7, v113, v66
	v_mfma_f32_32x32x16_f16 v[18:33], v[94:97], v[122:125], v[18:33]
	v_max3_f32 v7, v7, v67, v68
	v_max3_f32 v7, v7, v69, v70
	v_max3_f32 v7, v7, v71, v72
	v_max3_f32 v7, v7, v73, v74
	v_max3_f32 v7, v7, v75, v76
	v_max3_f32 v7, v7, v77, v78
	v_max3_f32 v7, v7, v79, v80
	v_mfma_f32_32x32x16_f16 v[82:97], v[136:139], v[118:121], 0
	v_max3_f32 v7, v7, v81, v50
	v_max3_f32 v7, v7, v51, v52
	v_max3_f32 v7, v7, v53, v54
	v_max3_f32 v7, v7, v55, v56
	v_max3_f32 v7, v7, v57, v58
	v_max3_f32 v7, v7, v59, v60
	v_max3_f32 v7, v7, v61, v62
	v_mfma_f32_32x32x16_f16 v[82:97], v[140:143], v[114:117], v[82:97]
	v_max3_f32 v7, v7, v63, v64
	v_max3_f32 v7, v7, v65, v34
	v_max3_f32 v7, v7, v35, v36
	v_max3_f32 v7, v7, v37, v38
	v_max3_f32 v7, v7, v39, v40
	v_max3_f32 v7, v7, v41, v42
	v_max3_f32 v7, v7, v43, v44
	s_waitcnt lgkmcnt(1)
	v_mfma_f32_32x32x16_f16 v[82:97], v[148:151], v[126:129], v[82:97]
	v_max3_f32 v7, v7, v45, v46
	v_max3_f32 v7, v7, v47, v48
	v_max3_f32 v7, v7, v49, v18
	v_max3_f32 v7, v7, v19, v20
	v_max3_f32 v7, v7, v21, v22
	v_max3_f32 v7, v7, v23, v24
	v_max3_f32 v7, v7, v25, v26
	s_waitcnt lgkmcnt(0)
	v_mfma_f32_32x32x16_f16 v[82:97], v[152:155], v[122:125], v[82:97]
	v_max3_f32 v7, v7, v27, v28
	v_max3_f32 v7, v7, v29, v30
	v_max3_f32 v7, v7, v31, v32
	s_nop 8
	v_max3_f32 v7, v7, v33, v82
	v_max3_f32 v7, v7, v83, v84
	v_max3_f32 v7, v7, v85, v86
	v_max3_f32 v7, v7, v87, v88
	v_max3_f32 v7, v7, v89, v90
	v_max3_f32 v7, v7, v91, v92
	v_max3_f32 v7, v7, v93, v94
	v_max3_f32 v7, v7, v95, v96
	v_max3_f32 v7, v7, v97, v2
	v_max3_f32 v7, v7, v3, v4
	v_max3_f32 v8, v7, v5, s3
	v_lshlrev_b32_e32 v7, 2, v6
	ds_bpermute_b32 v6, v7, v8
	s_mov_b32 s3, 0x3e38aa3b
	s_waitcnt lgkmcnt(0)
	v_max_f32_e32 v6, v6, v6
	v_max_f32_e32 v8, v8, v6
	v_mul_f32_e32 v6, 0x3e38aa3b, v8
	v_fma_f32 v9, v98, s3, -v6
	v_fma_f32 v10, v99, s3, -v6
	v_fma_f32 v167, v2, s3, -v6
	v_exp_f32_e32 v2, v9
	v_fma_f32 v11, v100, s3, -v6
	v_fmac_f32_e32 v168, 0xbe38aa3b, v8
	v_exp_f32_e32 v8, v10
	v_fma_f32 v12, v101, s3, -v6
	v_exp_f32_e32 v9, v11
	v_fma_f32 v13, v102, s3, -v6
	v_exp_f32_e32 v10, v12
	v_exp_f32_e32 v11, v13
	v_add_f32_e32 v12, 0, v2
	v_add_f32_e32 v12, v12, v8
	v_add_f32_e32 v12, v12, v9
	v_fma_f32 v14, v103, s3, -v6
	v_add_f32_e32 v12, v12, v10
	v_fma_f32 v15, v104, s3, -v6
	v_fma_f32 v151, v82, s3, -v6
	v_add_f32_e32 v82, v12, v11
	v_exp_f32_e32 v12, v14
	v_fma_f32 v16, v105, s3, -v6
	v_exp_f32_e32 v13, v15
	v_fma_f32 v17, v106, s3, -v6
	v_exp_f32_e32 v14, v16
	v_fma_f32 v98, v107, s3, -v6
	v_exp_f32_e32 v141, v17
	v_fma_f32 v99, v108, s3, -v6
	v_add_f32_e32 v15, v82, v12
	v_exp_f32_e32 v144, v98
	v_fma_f32 v100, v109, s3, -v6
	v_add_f32_e32 v15, v15, v13
	v_exp_f32_e32 v145, v99
	v_fma_f32 v101, v110, s3, -v6
	v_add_f32_e32 v15, v15, v14
	v_exp_f32_e32 v146, v100
	v_fma_f32 v102, v111, s3, -v6
	v_add_f32_e32 v15, v15, v141
	v_exp_f32_e32 v147, v101
	v_fma_f32 v103, v112, s3, -v6
	v_add_f32_e32 v15, v15, v144
	v_exp_f32_e32 v148, v102
	v_fma_f32 v104, v113, s3, -v6
	v_add_f32_e32 v15, v15, v145
	v_exp_f32_e32 v149, v103
	v_fma_f32 v66, v66, s3, -v6
	v_add_f32_e32 v15, v15, v146
	v_exp_f32_e32 v150, v104
	v_fma_f32 v67, v67, s3, -v6
	v_add_f32_e32 v15, v15, v147
	v_exp_f32_e32 v110, v66
	v_fma_f32 v68, v68, s3, -v6
	v_add_f32_e32 v15, v15, v148
	v_exp_f32_e32 v136, v67
	v_fma_f32 v69, v69, s3, -v6
	v_add_f32_e32 v15, v15, v149
	v_exp_f32_e32 v137, v68
	v_fma_f32 v70, v70, s3, -v6
	v_add_f32_e32 v15, v15, v150
	v_exp_f32_e32 v138, v69
	v_fma_f32 v71, v71, s3, -v6
	v_add_f32_e32 v15, v15, v110
	v_exp_f32_e32 v139, v70
	v_fma_f32 v72, v72, s3, -v6
	v_add_f32_e32 v15, v15, v136
	v_exp_f32_e32 v140, v71
	v_fma_f32 v73, v73, s3, -v6
	v_add_f32_e32 v15, v15, v137
	v_exp_f32_e32 v142, v72
	v_fma_f32 v74, v74, s3, -v6
	v_add_f32_e32 v15, v15, v138
	v_exp_f32_e32 v143, v73
	v_fma_f32 v75, v75, s3, -v6
	v_add_f32_e32 v15, v15, v139
	v_exp_f32_e32 v102, v74
	v_fma_f32 v76, v76, s3, -v6
	v_add_f32_e32 v15, v15, v140
	v_exp_f32_e32 v106, v75
	v_fma_f32 v77, v77, s3, -v6
	v_add_f32_e32 v15, v15, v142
	v_exp_f32_e32 v107, v76
	v_fma_f32 v78, v78, s3, -v6
	v_add_f32_e32 v15, v15, v143
	v_exp_f32_e32 v108, v77
	v_fma_f32 v79, v79, s3, -v6
	v_add_f32_e32 v15, v15, v102
	v_exp_f32_e32 v109, v78
	v_fma_f32 v80, v80, s3, -v6
	v_add_f32_e32 v15, v15, v106
	v_exp_f32_e32 v111, v79
	v_fma_f32 v81, v81, s3, -v6
	v_add_f32_e32 v15, v15, v107
	v_exp_f32_e32 v112, v80
	v_fma_f32 v50, v50, s3, -v6
	v_add_f32_e32 v15, v15, v108
	v_exp_f32_e32 v113, v81
	v_fma_f32 v51, v51, s3, -v6
	v_fma_f32 v163, v94, s3, -v6
	v_add_f32_e32 v15, v15, v109
	v_exp_f32_e32 v94, v50
	v_fma_f32 v52, v52, s3, -v6
	v_add_f32_e32 v15, v15, v111
	v_exp_f32_e32 v98, v51
	v_fma_f32 v53, v53, s3, -v6
	v_add_f32_e32 v15, v15, v112
	v_exp_f32_e32 v99, v52
	v_fma_f32 v54, v54, s3, -v6
	v_add_f32_e32 v15, v15, v113
	v_exp_f32_e32 v100, v53
	v_fma_f32 v55, v55, s3, -v6
	v_add_f32_e32 v15, v15, v94
	v_exp_f32_e32 v101, v54
	v_fma_f32 v56, v56, s3, -v6
	v_add_f32_e32 v15, v15, v98
	v_exp_f32_e32 v103, v55
	v_fma_f32 v57, v57, s3, -v6
	v_add_f32_e32 v15, v15, v99
	v_exp_f32_e32 v104, v56
	v_fma_f32 v58, v58, s3, -v6
	v_add_f32_e32 v15, v15, v100
	v_exp_f32_e32 v105, v57
	v_fma_f32 v59, v59, s3, -v6
	v_fma_f32 v155, v86, s3, -v6
	v_add_f32_e32 v15, v15, v101
	v_exp_f32_e32 v86, v58
	v_fma_f32 v60, v60, s3, -v6
	v_fma_f32 v159, v90, s3, -v6
	v_add_f32_e32 v15, v15, v103
	v_exp_f32_e32 v90, v59
	v_fma_f32 v61, v61, s3, -v6
	v_fma_f32 v160, v91, s3, -v6
	v_add_f32_e32 v15, v15, v104
	v_exp_f32_e32 v91, v60
	v_fma_f32 v62, v62, s3, -v6
	v_fma_f32 v161, v92, s3, -v6
	v_add_f32_e32 v15, v15, v105
	v_exp_f32_e32 v92, v61
	v_fma_f32 v63, v63, s3, -v6
	v_fma_f32 v162, v93, s3, -v6
	v_add_f32_e32 v15, v15, v86
	v_exp_f32_e32 v93, v62
	v_fma_f32 v64, v64, s3, -v6
	v_fma_f32 v164, v95, s3, -v6
	v_add_f32_e32 v15, v15, v90
	v_exp_f32_e32 v95, v63
	v_fma_f32 v65, v65, s3, -v6
	v_fma_f32 v165, v96, s3, -v6
	v_add_f32_e32 v15, v15, v91
	v_exp_f32_e32 v96, v64
	v_fma_f32 v34, v34, s3, -v6
	v_fma_f32 v166, v97, s3, -v6
	v_add_f32_e32 v15, v15, v92
	v_exp_f32_e32 v97, v65
	v_fma_f32 v35, v35, s3, -v6
	v_add_f32_e32 v15, v15, v93
	v_exp_f32_e32 v78, v34
	v_fma_f32 v36, v36, s3, -v6
	v_add_f32_e32 v15, v15, v95
	v_exp_f32_e32 v82, v35
	v_fma_f32 v37, v37, s3, -v6
	v_fma_f32 v152, v83, s3, -v6
	v_add_f32_e32 v15, v15, v96
	v_exp_f32_e32 v83, v36
	v_fma_f32 v38, v38, s3, -v6
	v_fma_f32 v153, v84, s3, -v6
	v_add_f32_e32 v15, v15, v97
	v_exp_f32_e32 v84, v37
	v_fma_f32 v39, v39, s3, -v6
	v_fma_f32 v154, v85, s3, -v6
	v_add_f32_e32 v15, v15, v78
	v_exp_f32_e32 v85, v38
	v_fma_f32 v40, v40, s3, -v6
	v_fma_f32 v156, v87, s3, -v6
	v_add_f32_e32 v15, v15, v82
	v_exp_f32_e32 v87, v39
	v_fma_f32 v41, v41, s3, -v6
	v_fma_f32 v157, v88, s3, -v6
	v_add_f32_e32 v15, v15, v83
	v_exp_f32_e32 v88, v40
	v_fma_f32 v42, v42, s3, -v6
	v_fma_f32 v158, v89, s3, -v6
	v_add_f32_e32 v15, v15, v84
	v_exp_f32_e32 v89, v41
	v_fma_f32 v43, v43, s3, -v6
	v_add_f32_e32 v15, v15, v85
	v_exp_f32_e32 v70, v42
	v_fma_f32 v44, v44, s3, -v6
	v_add_f32_e32 v15, v15, v87
	v_exp_f32_e32 v74, v43
	v_fma_f32 v45, v45, s3, -v6
	v_add_f32_e32 v15, v15, v88
	v_exp_f32_e32 v75, v44
	v_fma_f32 v46, v46, s3, -v6
	v_add_f32_e32 v15, v15, v89
	v_exp_f32_e32 v76, v45
	v_fma_f32 v47, v47, s3, -v6
	v_add_f32_e32 v15, v15, v70
	v_exp_f32_e32 v77, v46
	v_fma_f32 v48, v48, s3, -v6
	v_add_f32_e32 v15, v15, v74
	v_exp_f32_e32 v79, v47
	v_fma_f32 v49, v49, s3, -v6
	v_add_f32_e32 v15, v15, v75
	v_exp_f32_e32 v80, v48
	v_fma_f32 v18, v18, s3, -v6
	v_add_f32_e32 v15, v15, v76
	v_exp_f32_e32 v81, v49
	v_fma_f32 v19, v19, s3, -v6
	v_add_f32_e32 v15, v15, v77
	v_exp_f32_e32 v63, v18
	v_fma_f32 v20, v20, s3, -v6
	v_add_f32_e32 v15, v15, v79
	v_exp_f32_e32 v66, v19
	v_fma_f32 v21, v21, s3, -v6
	v_add_f32_e32 v15, v15, v80
	v_exp_f32_e32 v67, v20
	v_fma_f32 v22, v22, s3, -v6
	v_add_f32_e32 v15, v15, v81
	v_exp_f32_e32 v68, v21
	v_fma_f32 v23, v23, s3, -v6
	v_add_f32_e32 v15, v15, v63
	v_exp_f32_e32 v69, v22
	v_fma_f32 v24, v24, s3, -v6
	v_add_f32_e32 v15, v15, v66
	v_exp_f32_e32 v71, v23
	v_fma_f32 v25, v25, s3, -v6
	v_add_f32_e32 v15, v15, v67
	v_exp_f32_e32 v72, v24
	v_fma_f32 v26, v26, s3, -v6
	v_add_f32_e32 v15, v15, v68
	v_exp_f32_e32 v73, v25
	v_fma_f32 v27, v27, s3, -v6
	v_add_f32_e32 v15, v15, v69
	v_exp_f32_e32 v54, v26
	v_fma_f32 v28, v28, s3, -v6
	v_add_f32_e32 v15, v15, v71
	v_exp_f32_e32 v58, v27
	v_fma_f32 v29, v29, s3, -v6
	v_add_f32_e32 v15, v15, v72
	v_exp_f32_e32 v59, v28
	v_fma_f32 v30, v30, s3, -v6
	v_add_f32_e32 v15, v15, v73
	v_exp_f32_e32 v60, v29
	v_fma_f32 v31, v31, s3, -v6
	v_add_f32_e32 v15, v15, v54
	v_exp_f32_e32 v61, v30
	v_fma_f32 v32, v32, s3, -v6
	v_add_f32_e32 v15, v15, v58
	v_exp_f32_e32 v62, v31
	v_fma_f32 v33, v33, s3, -v6
	v_add_f32_e32 v15, v15, v59
	v_exp_f32_e32 v64, v32
	v_add_f32_e32 v15, v15, v60
	v_exp_f32_e32 v65, v33
	v_add_f32_e32 v15, v15, v61
	v_exp_f32_e32 v46, v151
	v_add_f32_e32 v15, v15, v62
	v_exp_f32_e32 v50, v152
	v_add_f32_e32 v15, v15, v64
	v_exp_f32_e32 v51, v153
	v_add_f32_e32 v15, v15, v65
	v_exp_f32_e32 v52, v154
	v_add_f32_e32 v15, v15, v46
	v_exp_f32_e32 v53, v155
	v_add_f32_e32 v15, v15, v50
	v_exp_f32_e32 v55, v156
	v_add_f32_e32 v15, v15, v51
	v_exp_f32_e32 v56, v157
	v_add_f32_e32 v15, v15, v52
	v_exp_f32_e32 v57, v158
	v_add_f32_e32 v15, v15, v53
	v_exp_f32_e32 v40, v159
	v_add_f32_e32 v15, v15, v55
	v_exp_f32_e32 v42, v160
	v_add_f32_e32 v15, v15, v56
	v_exp_f32_e32 v43, v161
	v_add_f32_e32 v15, v15, v57
	v_exp_f32_e32 v44, v162
	v_add_f32_e32 v15, v15, v40
	v_exp_f32_e32 v45, v163
	v_add_f32_e32 v15, v15, v42
	v_exp_f32_e32 v47, v164
	v_add_f32_e32 v15, v15, v43
	v_exp_f32_e32 v48, v165
	v_add_f32_e32 v15, v15, v44
	v_exp_f32_e32 v49, v166
	v_add_f32_e32 v15, v15, v45
	v_exp_f32_e32 v36, v167
	v_fma_f32 v3, v3, s3, -v6
	v_add_f32_e32 v15, v15, v47
	v_exp_f32_e32 v37, v3
	v_fma_f32 v3, v4, s3, -v6
	v_add_f32_e32 v15, v15, v48
	v_exp_f32_e32 v38, v3
	v_fma_f32 v3, v5, s3, -v6
	v_add_f32_e32 v15, v15, v49
	v_exp_f32_e32 v41, v3
	v_add_f32_e32 v15, v15, v36
	v_exp_f32_e32 v39, v168
	v_add_f32_e32 v3, v15, v37
	v_add_f32_e32 v3, v3, v38
	v_add_f32_e32 v3, v3, v41
	v_add_f32_e32 v3, v3, v39
	v_add_f32_e32 v3, v3, v39
	v_add_f32_e32 v3, v3, v39
	v_add_f32_e32 v3, v3, v39
	v_add_f32_e32 v3, v3, v39
	v_add_f32_e32 v3, v3, v39
	v_add_f32_e32 v3, v3, v39
	v_add_f32_e32 v3, v3, v39
	v_add_f32_e32 v3, v3, v39
	v_add_f32_e32 v3, v3, v39
	v_add_f32_e32 v3, v3, v39
	v_add_f32_e32 v3, v3, v39
	ds_bpermute_b32 v4, v7, v3
	v_lshlrev_b32_e32 v35, 3, v1
	s_waitcnt lgkmcnt(0)
	v_add_f32_e32 v34, v3, v4
	s_and_saveexec_b64 s[10:11], s[6:7]
	s_cbranch_execz .LBB3_6
	s_mov_b32 s3, 0x800000
	v_cmp_gt_f32_e32 vcc, s3, v34
	v_mov_b32_e32 v3, 0x42000000
	v_lshlrev_b32_e32 v5, 2, v135
	v_cndmask_b32_e64 v4, 0, 32, vcc
	v_ldexp_f32 v4, v34, v4
	v_log_f32_e32 v4, v4
	v_cndmask_b32_e32 v3, 0, v3, vcc
	v_sub_f32_e32 v3, v4, v3
	v_add_f32_e32 v3, v6, v3
	ds_write_b32 v5, v3 offset:61440
